# speedup vs baseline: 1.0111x; 1.0111x over previous
.LBB3_11:
	s_and_b64 vcc, exec, s[4:5]
	s_cbranch_vccz .LBB3_14
	s_add_i32 s19, s2, 0xfffffe00
	s_load_dwordx2 s[20:21], s[0:1], 0x88
	s_load_dwordx2 s[22:23], s[0:1], 0xc0
	s_load_dwordx2 s[24:25], s[0:1], 0xf8
	s_load_dwordx2 s[26:27], s[0:1], 0x130
	s_load_dwordx2 s[28:29], s[0:1], 0x168
	s_load_dwordx4 s[32:35], s[0:1], 0x1a0
	s_mov_b32 s3, 0
	s_waitcnt lgkmcnt(0)
	s_cmp_ge_i32 s19, s20
	s_cselect_b32 s36, 1, 0
	s_cmp_gt_i32 s34, 1
	s_cselect_b32 s37, 1, 0
	s_and_b32 s36, s36, s37
	s_cselect_b32 s3, 1, s3
	s_cmp_ge_i32 s19, s22
	s_cselect_b32 s36, 1, 0
	s_cmp_gt_i32 s34, 2
	s_cselect_b32 s37, 1, 0
	s_and_b32 s36, s36, s37
	s_cselect_b32 s3, 2, s3
	s_cmp_ge_i32 s19, s24
	s_cselect_b32 s36, 1, 0
	s_cmp_gt_i32 s34, 3
	s_cselect_b32 s37, 1, 0
	s_and_b32 s36, s36, s37
	s_cselect_b32 s3, 3, s3
	s_cmp_ge_i32 s19, s26
	s_cselect_b32 s36, 1, 0
	s_cmp_gt_i32 s34, 4
	s_cselect_b32 s37, 1, 0
	s_and_b32 s36, s36, s37
	s_cselect_b32 s3, 4, s3
	s_cmp_ge_i32 s19, s28
	s_cselect_b32 s36, 1, 0
	s_cmp_gt_i32 s34, 5
	s_cselect_b32 s37, 1, 0
	s_and_b32 s36, s36, s37
	s_cselect_b32 s3, 5, s3
	s_cmp_ge_i32 s19, s32
	s_cselect_b32 s36, 1, 0
	s_cmp_gt_i32 s34, 6
	s_cselect_b32 s37, 1, 0
	s_and_b32 s36, s36, s37
	s_cselect_b32 s3, 6, s3
	s_mul_i32 s36, s3, 56
	s_add_i32 s36, s36, 32
	s_add_i32 s37, s36, 32
	s_add_i32 s38, s36, 48
	s_load_dwordx8 s[4:11], s[0:1], s36
	s_load_dwordx4 s[12:15], s[0:1], s37
	s_load_dwordx2 s[20:21], s[0:1], s38
	s_waitcnt lgkmcnt(0)
	s_mov_b32 s2, s20
	s_mul_i32 s0, s10, s11
	s_abs_i32 s1, s0
	v_cvt_f32_u32_e32 v0, s1
	s_sub_i32 s16, 0, s1
	s_sub_i32 s2, s19, s2
	s_add_i32 s2, s2, s21
	v_rcp_iflag_f32_e32 v0, v0
	s_abs_i32 s11, s2
	s_xor_b32 s3, s2, s0
	s_ashr_i32 s3, s3, 31
	v_mul_f32_e32 v0, 0x4f7ffffe, v0
	v_cvt_u32_f32_e32 v0, v0
	v_and_b32_e32 v36, 0xf0, v10
	v_mov_b32_e32 v37, 0
	v_readfirstlane_b32 s17, v0
	s_mul_i32 s16, s16, s17
	s_mul_hi_u32 s16, s17, s16
	s_add_i32 s17, s17, s16
	s_mul_hi_u32 s16, s11, s17
	s_mul_i32 s17, s16, s1
	s_sub_i32 s11, s11, s17
	s_add_i32 s18, s16, 1
	s_sub_i32 s17, s11, s1
	s_cmp_ge_u32 s11, s1
	s_cselect_b32 s16, s18, s16
	s_cselect_b32 s11, s17, s11
	s_add_i32 s17, s16, 1
	s_cmp_ge_u32 s11, s1
	s_cselect_b32 s1, s17, s16
	s_abs_i32 s11, s10
	v_cvt_f32_u32_e32 v0, s11
	s_xor_b32 s1, s1, s3
	s_sub_i32 s16, 0, s11
	s_sub_i32 s3, s1, s3
	v_rcp_iflag_f32_e32 v0, v0
	s_mul_i32 s0, s3, s0
	s_sub_i32 s0, s2, s0
	s_abs_i32 s2, s0
	v_mul_f32_e32 v0, 0x4f7ffffe, v0
	v_cvt_u32_f32_e32 v0, v0
	s_xor_b32 s1, s0, s10
	s_ashr_i32 s1, s1, 31
	v_readfirstlane_b32 s17, v0
	s_mul_i32 s16, s16, s17
	s_mul_hi_u32 s16, s17, s16
	s_add_i32 s17, s17, s16
	s_mul_hi_u32 s16, s2, s17
	s_mul_i32 s17, s16, s11
	s_sub_i32 s2, s2, s17
	s_add_i32 s18, s16, 1
	s_sub_i32 s17, s2, s11
	s_cmp_ge_u32 s2, s11
	s_cselect_b32 s16, s18, s16
	s_cselect_b32 s2, s17, s2
	s_add_i32 s17, s16, 1
	s_cmp_ge_u32 s2, s11
	s_cselect_b32 s2, s17, s16
	s_xor_b32 s2, s2, s1
	s_sub_i32 s2, s2, s1
	s_mul_i32 s1, s2, s10
	s_ashr_i32 s11, s3, 31
	s_sub_i32 s10, s0, s1
	s_mul_i32 s0, s12, s11
	s_mul_hi_u32 s1, s12, s3
	s_add_i32 s0, s1, s0
	s_mul_i32 s1, s13, s3
	s_add_i32 s1, s0, s1
	s_mul_i32 s0, s12, s3
	s_lshl_b64 s[0:1], s[0:1], 2
	s_add_u32 s4, s4, s0
	s_addc_u32 s12, s5, s1
	s_mul_i32 s0, s14, s11
	s_mul_hi_u32 s1, s14, s3
	s_add_i32 s0, s1, s0
	s_mul_i32 s1, s15, s3
	s_add_i32 s5, s0, s1
	s_lshl_b32 s0, s10, 6
	s_ashr_i32 s1, s0, 31
	s_lshl_b32 s2, s2, 7
	s_lshl_b64 s[10:11], s[0:1], 2
	s_add_u32 s10, s4, s10
	v_or_b32_e32 v28, s2, v29
	s_addc_u32 s11, s12, s11
	v_lshl_add_u64 v[32:33], s[10:11], 0, v[36:37]
	v_mad_i64_i32 v[0:1], s[10:11], v28, s9, 0
	v_lshl_add_u64 v[8:9], v[0:1], 2, v[32:33]
	v_or_b32_e32 v0, 16, v28
	v_mad_i64_i32 v[0:1], s[10:11], v0, s9, 0
	v_lshl_add_u64 v[10:11], v[0:1], 2, v[32:33]
	global_load_dwordx4 v[0:3], v[8:9], off nt
	global_load_dwordx4 v[4:7], v[10:11], off nt
	v_or_b32_e32 v8, 32, v28
	v_mad_i64_i32 v[8:9], s[10:11], v8, s9, 0
	v_lshl_add_u64 v[16:17], v[8:9], 2, v[32:33]
	v_or_b32_e32 v8, 48, v28
	v_mad_i64_i32 v[8:9], s[10:11], v8, s9, 0
	v_lshl_add_u64 v[18:19], v[8:9], 2, v[32:33]
	global_load_dwordx4 v[8:11], v[16:17], off nt
	global_load_dwordx4 v[12:15], v[18:19], off nt
	v_or_b32_e32 v16, 64, v28
	v_mad_i64_i32 v[16:17], s[10:11], v16, s9, 0
	v_lshl_add_u64 v[24:25], v[16:17], 2, v[32:33]
	v_or_b32_e32 v16, 0x50, v28
	v_mad_i64_i32 v[16:17], s[10:11], v16, s9, 0
	v_lshl_add_u64 v[26:27], v[16:17], 2, v[32:33]
	global_load_dwordx4 v[16:19], v[24:25], off nt
	global_load_dwordx4 v[20:23], v[26:27], off nt
	v_or_b32_e32 v24, 0x60, v28
	v_mad_i64_i32 v[24:25], s[10:11], v24, s9, 0
	v_lshl_add_u64 v[24:25], v[24:25], 2, v[32:33]
	v_or_b32_e32 v28, 0x70, v28
	global_load_dwordx4 v[24:27], v[24:25], off nt
	v_mad_i64_i32 v[34:35], s[10:11], v28, s9, 0
	v_lshl_add_u64 v[32:33], v[34:35], 2, v[32:33]
	global_load_dwordx4 v[32:35], v[32:33], off nt
	s_movk_i32 s1, 0x104
	v_mad_u32_u24 v28, v29, s1, v36
	v_add_u32_e32 v31, 0x1040, v28
	v_add_u32_e32 v36, 0x1048, v28
	v_add_u32_e32 v38, 0x2080, v28
	v_add_u32_e32 v39, 0x2088, v28
	v_add_u32_e32 v40, 0x30c0, v28
	v_add_u32_e32 v41, 0x30c8, v28
	v_add_u32_e32 v42, 0x4100, v28
	v_add_u32_e32 v43, 0x4108, v28
	v_add_u32_e32 v44, 0x5140, v28
	v_add_u32_e32 v45, 0x5148, v28
	s_mul_i32 s4, s14, s3
	s_lshl_b64 s[4:5], s[4:5], 1
	s_add_u32 s1, s6, s4
	s_addc_u32 s4, s7, s5
	s_ashr_i32 s3, s2, 31
	s_lshl_b64 s[2:3], s[2:3], 1
	s_add_u32 s2, s1, s2
	s_addc_u32 s3, s4, s3
	s_waitcnt vmcnt(7)
	ds_write2_b32 v28, v0, v1 offset1:1
	ds_write2_b32 v28, v2, v3 offset0:2 offset1:3
	s_waitcnt vmcnt(6)
	ds_write2_b32 v31, v4, v5 offset1:1
	ds_write2_b32 v36, v6, v7 offset1:1
	s_waitcnt vmcnt(5)
	ds_write2_b32 v38, v8, v9 offset1:1
	ds_write2_b32 v39, v10, v11 offset1:1
	s_waitcnt vmcnt(4)
	ds_write2_b32 v40, v12, v13 offset1:1
	ds_write2_b32 v41, v14, v15 offset1:1
	s_waitcnt vmcnt(3)
	ds_write2_b32 v42, v16, v17 offset1:1
	ds_write2_b32 v43, v18, v19 offset1:1
	s_waitcnt vmcnt(2)
	ds_write2_b32 v44, v20, v21 offset1:1
	ds_write2_b32 v45, v22, v23 offset1:1
	v_add_u32_e32 v0, 0x6180, v28
	s_waitcnt vmcnt(1)
	ds_write2_b32 v0, v24, v25 offset1:1
	v_add_u32_e32 v0, 0x6188, v28
	ds_write2_b32 v0, v26, v27 offset1:1
	v_add_u32_e32 v0, 0x71c0, v28
	s_waitcnt vmcnt(0)
	ds_write2_b32 v0, v32, v33 offset1:1
	v_add_u32_e32 v0, 0x71c8, v28
	ds_write2_b32 v0, v34, v35 offset1:1
	v_and_b32_e32 v0, 0x78, v30
	v_lshlrev_b32_e32 v36, 1, v0
	v_mul_u32_u24_e32 v0, 0x104, v0
	v_lshl_add_u32 v24, v29, 2, v0
	v_add_u32_e32 v25, 0x400, v24
	s_waitcnt lgkmcnt(0)
	s_barrier
	ds_read2_b32 v[4:5], v24 offset1:16
	ds_read2_b32 v[6:7], v24 offset0:130 offset1:146
	ds_read2_b32 v[8:9], v25 offset0:4 offset1:20
	ds_read2_b32 v[10:11], v25 offset0:134 offset1:150
	ds_read2_b32 v[12:13], v25 offset0:199 offset1:215
	ds_read2_b32 v[14:15], v25 offset0:69 offset1:85
	ds_read2_b32 v[16:17], v24 offset0:195 offset1:211
	ds_read2_b32 v[18:19], v24 offset0:65 offset1:81
	v_or_b32_e32 v26, s0, v29
	v_lshl_add_u64 v[20:21], s[2:3], 0, v[36:37]
	v_mad_i64_i32 v[22:23], s[0:1], v26, s8, 0
	s_waitcnt lgkmcnt(3)
	v_cvt_pk_f16_f32 v3, v10, v12
	s_waitcnt lgkmcnt(2)
	v_cvt_pk_f16_f32 v2, v8, v14
	s_waitcnt lgkmcnt(1)
	v_cvt_pk_f16_f32 v1, v6, v16
	s_waitcnt lgkmcnt(0)
	v_cvt_pk_f16_f32 v0, v4, v18
	v_lshl_add_u64 v[22:23], v[22:23], 1, v[20:21]
	global_store_dwordx4 v[22:23], v[0:3], off sc1
	v_or_b32_e32 v4, 16, v26
	s_nop 0
	v_cvt_pk_f16_f32 v3, v11, v13
	v_cvt_pk_f16_f32 v2, v9, v15
	v_cvt_pk_f16_f32 v1, v7, v17
	v_cvt_pk_f16_f32 v0, v5, v19
	ds_read2_b32 v[6:7], v24 offset0:32 offset1:48
	ds_read2_b32 v[8:9], v24 offset0:162 offset1:178
	ds_read2_b32 v[10:11], v25 offset0:36 offset1:52
	ds_read2_b32 v[12:13], v25 offset0:166 offset1:182
	ds_read2_b32 v[14:15], v25 offset0:231 offset1:247
	ds_read2_b32 v[16:17], v25 offset0:101 offset1:117
	ds_read2_b32 v[18:19], v24 offset0:227 offset1:243
	ds_read2_b32 v[22:23], v24 offset0:97 offset1:113
	v_mad_i64_i32 v[4:5], s[0:1], v4, s8, 0
	v_lshl_add_u64 v[4:5], v[4:5], 1, v[20:21]
	global_store_dwordx4 v[4:5], v[0:3], off sc1
	v_or_b32_e32 v4, 32, v26
	v_mad_i64_i32 v[4:5], s[0:1], v4, s8, 0
	s_waitcnt lgkmcnt(3)
	v_cvt_pk_f16_f32 v3, v12, v14
	s_waitcnt lgkmcnt(2)
	v_cvt_pk_f16_f32 v2, v10, v16
	s_waitcnt lgkmcnt(1)
	v_cvt_pk_f16_f32 v1, v8, v18
	s_waitcnt lgkmcnt(0)
	v_cvt_pk_f16_f32 v0, v6, v22
	v_lshl_add_u64 v[4:5], v[4:5], 1, v[20:21]
	global_store_dwordx4 v[4:5], v[0:3], off sc1
	v_or_b32_e32 v4, 48, v26
	v_mad_i64_i32 v[4:5], s[0:1], v4, s8, 0
	v_cvt_pk_f16_f32 v3, v13, v15
	v_cvt_pk_f16_f32 v2, v11, v17
	v_cvt_pk_f16_f32 v1, v9, v19
	v_cvt_pk_f16_f32 v0, v7, v23
	v_lshl_add_u64 v[4:5], v[4:5], 1, v[20:21]
	global_store_dwordx4 v[4:5], v[0:3], off sc1
	s_endpgm
